# cross-unit de-serialisation: a unit's completion count is published at the next unit's landed-barrier, so its write-through O stores drain behind the next unit's K/V DMA and Q loads (redundant vmcnt(0
# baseline (speedup 1.0000x reference)
; __device__ __forceinline__ int obid() { int t = blockIdx.x; asm volatile("" : "+s"(t)); return t; }
; __device__ __forceinline__ int ogrid() { int t = gridDim.x; asm volatile("" : "+s"(t)); return t; }
; __device__ __forceinline__ CParams* kparams() { CParams* k = (CParams*)__builtin_amdgcn_kernarg_segment_ptr(); asm volatile("" : "+s"(k)); return k; }
; __global__ void __launch_bounds__(512, 2) mk_fwd(Params p_unused) {
;     ...
;     if (IN(4)) _Pragma("unroll 1") for (int rep_ = 0; rep_ < NREP(4); ++rep_) {
;         CParams* kp = kparams();
;         const bf16_t* Qb = WSP(bf16_t, WS_Q); const bf16_t* Kb = WSP(bf16_t, WS_K); const bf16_t* Vb = WSP(bf16_t, WS_V); bf16_t* Ob = WSP(bf16_t, WS_O);
;         const bf16_t* QKVR = WSP(bf16_t, WS_QKVR); const float* ROPE = WSP(float, WS_ROPE); const float* qgn = kp->q_gain;
;         const int G = ogrid(), bx = obid(); const bool fast = (G % 8) == 0;
;         const int NR = fast ? (G >> 3) : G, rank = fast ? (bx >> 3) : bx, tot = fast ? 132 : 1056;
;         const bool split = fast && NR == 32; const int NA = split ? 26 : NR;
;         if (rank < NA) for (int i = 0;; ++i) {
;             int w = rank + NA * i;
;             if (split && i == 5) w = rank >= 24 ? rank + 106 : tot;
;             if (w >= tot) break;
;             const int combo = fast ? (bx & 7) : (w / 132), ww = fast ? w : (w % 132), b = combo >> 2, kvh = combo & 3;
;             const bool isl = ww < 128; const int rbk = ww >> 2; const int h = kvh * 4 + (isl ? (ww & 3) : (ww - 128));
;             const size_t row0 = isl ? ((size_t)NCTX + (size_t)b * SEQ + (size_t)rbk * 256) : ((size_t)b * CTXL);
;             if (isl) att::attn_dma_body(QKVR + row0 * QKVD + h * HD, QKVD, rbk * 256, ROPE, qgn, Kb + (size_t)combo * SKV * HD, Vb + (size_t)combo * SKV * HD, Ob + row0 * DM + h * HD, SKV, (char*)lds);
.LBB0_372:
	s_cmp_gt_i32 s54, 4
	s_cselect_b64 s[4:5], -1, 0
	s_xor_b64 s[2:3], s[2:3], -1
	s_or_b64 s[2:3], s[4:5], s[2:3]
	s_and_b64 vcc, exec, s[2:3]
	s_cbranch_vccnz .LBB0_557
	s_mov_b64 s[30:31], s[0:1]
	s_load_dword s33, s[0:1], 0xb0
	s_load_dwordx2 s[28:29], s[30:31], 0xa0
	s_mov_b32 s2, s96
	s_waitcnt lgkmcnt(0)
	s_mov_b32 s3, s33
	s_add_u32 s23, s28, 0x5f500000
	s_addc_u32 s94, s29, 0
	s_and_b32 s4, s3, 7
	s_ashr_i32 s6, s3, 3
	s_ashr_i32 s7, s2, 3
	s_cmp_eq_u32 s4, 0
	s_cselect_b64 s[10:11], -1, 0
	s_and_b64 s[4:5], s[10:11], exec
	s_cselect_b32 s3, s6, s3
	s_cselect_b32 s21, s7, s2
	s_cmp_eq_u32 s3, 32
	s_cselect_b64 s[4:5], -1, 0
	s_and_b64 s[12:13], s[10:11], s[4:5]
	s_and_b64 s[4:5], s[12:13], exec
	s_cselect_b32 s56, 26, s3
	s_cmp_ge_i32 s21, s56
	s_cbranch_scc1 .LBB0_440
	s_movk_i32 s3, 0x84
	s_and_b64 s[4:5], s[10:11], exec
	s_cselect_b32 s57, s3, 0x420
	s_cmp_ge_i32 s21, s57
	s_cbranch_scc1 .LBB0_440
	s_mov_b32 s101, 0
	s_load_dwordx4 s[4:7], s[30:31], 0x48
	v_and_b32_e32 v253, 63, v0
	v_lshlrev_b32_e32 v253, 2, v253
	s_waitcnt lgkmcnt(0)
	global_load_dword v251, v253, s[4:5]
	global_load_dword v254, v253, s[4:5] offset:256
	global_load_dword v252, v253, s[6:7]
	global_load_dword v255, v253, s[6:7] offset:256
	s_waitcnt vmcnt(0)
	v_max_f32_e64 v251, |v251|, |v254|
	v_max_f32_e64 v252, |v252|, |v255|
	s_nop 1
	v_max_f32_dpp v251, v251, v251 quad_perm:[1,0,3,2] row_mask:0xf bank_mask:0xf
	v_max_f32_dpp v252, v252, v252 quad_perm:[1,0,3,2] row_mask:0xf bank_mask:0xf
	s_nop 1
	v_max_f32_dpp v251, v251, v251 quad_perm:[2,3,0,1] row_mask:0xf bank_mask:0xf
	v_max_f32_dpp v252, v252, v252 quad_perm:[2,3,0,1] row_mask:0xf bank_mask:0xf
	s_nop 1
	v_max_f32_dpp v251, v251, v251 row_half_mirror row_mask:0xf bank_mask:0xf
	v_max_f32_dpp v252, v252, v252 row_half_mirror row_mask:0xf bank_mask:0xf
	s_nop 1
	v_max_f32_dpp v251, v251, v251 row_mirror row_mask:0xf bank_mask:0xf
	v_max_f32_dpp v252, v252, v252 row_mirror row_mask:0xf bank_mask:0xf
	v_max_f32_e32 v251, v251, v252
	s_nop 1
	v_readlane_b32 s4, v251, 0
	v_readlane_b32 s5, v251, 16
	v_readlane_b32 s6, v251, 32
	v_readlane_b32 s7, v251, 48
	s_nop 3
	s_max_u32 s4, s4, s5
	s_max_u32 s6, s6, s7
	s_max_u32 s4, s4, s6
	s_cmp_gt_u32 s4, 0x4019999a
	s_cselect_b32 s100, 1, 0
	s_add_i32 s3, s21, 0x6a
	s_cmp_gt_i32 s21, 23
	s_cselect_b32 s46, s3, s57
	s_add_u32 s47, s28, 0x59100000
	s_addc_u32 s48, s29, 0
	s_add_u32 s49, s28, 0x5d300000
	s_addc_u32 s50, s29, 0
	s_add_u32 s51, s28, 0x5e400000
	s_addc_u32 s93, s29, 0
	s_add_u32 s22, s28, 0x52e00000
	s_addc_u32 s88, s29, 0
	s_load_dwordx2 s[14:15], s[30:31], 0x48
	s_add_u32 s16, s28, 0x180000
	s_addc_u32 s17, s29, 0
	s_and_b32 s18, s2, 7
	s_add_u32 s19, s28, 0x8000
	s_addc_u32 s2, s29, 0
	v_writelane_b32 v250, s2, 6
	s_mov_b32 s73, 0
	v_mov_b32_e32 v163, 0
	s_mov_b32 s89, 0x42b504f3
	s_mov_b32 s20, 0x3e0293ee
	s_add_i32 s90, 0, 0x20500
	s_movk_i32 s91, 0x2200
	s_movk_i32 s92, 0x7fff
	s_mov_b64 s[24:25], 0x4040
	v_mov_b32_e32 v1, 0x358637bd
	v_mov_b32_e32 v174, 0x260
	s_mov_b64 s[26:27], 0x5d30c000
	s_mov_b64 s[58:59], 0x5e40c000
	s_mov_b64 s[60:61], 0x5d310000
	s_mov_b64 s[62:63], 0x5e410000
	v_mov_b32_e32 v175, 0xf149f2ca
	s_mov_b32 s2, s21
	s_mov_b32 s95, 0
	s_branch .LBB0_377

; __device__ __forceinline__ int otid() { int t = threadIdx.x; asm volatile("" : "+v"(t)); return t; }
; __device__ __forceinline__ void attn_dma_body(const bf16_t* __restrict__ Qb, int ldq, int tpos0, const float* __restrict__ rope, const float* __restrict__ qgain, ...
;   const int tid = otid(), wid = tid >> 6, lane = tid & 63, r32 = lane & 31, hi = lane >> 5;
;   float* ws = (float*)(lds + TAB_OFF + 1024) + wid * 64; float* li_l = ws; float* al_l = ws + 32;
;   float m_reg = -1e30f, l_reg = 0; f32x16 o[4] = {}; bf16x8 qr[8];
;   const bf16_t* Qw = Qb + (long)(wid * QBLK + r32) * ldq + hi * 8;
;   unsigned koff[2], voff[2];
; #pragma unroll
;   for (int c = 0; c < 2; ++c) { const int g = c * 512 + tid;
;     { const int row = g >> 4, ch = (g & 15) ^ (row & 7); koff[c] = (unsigned)(row * 128 + ch * 8) * 2u; }
;     { const int sub = g >> 5, kk = (sub >> 2) * 8 + ((g >> 2) & 7), k = (kk & ~0xC) | ((kk & 4) << 1) | ((kk & 8) >> 1), col = (sub & 3) * 32 + (g & 3) * 8; voff[c] = (unsigned)(k * 128 + col) * 2u; } }
;   const unsigned wbase = (unsigned)__builtin_amdgcn_readfirstlane(wid) * 1024u;
;   typedef __attribute__((address_space(3))) unsigned lds_u32;
;   lds_u32* ldsl = (lds_u32*)(__attribute__((address_space(3))) char*)lds;
;     ...
;   const int NT = seq / KVBLK;
;   ATT_DMA(0, 0); ATT_DMA(1, 1);
; #pragma unroll
;   for (int d0 = 0; d0 < 8; ++d0) qr[d0] = ld8(Qw + d0 * 16);
;   if (tpos0 >= 0) {
;     float ss = 0.f;
; #pragma unroll
;     for (int d0 = 0; d0 < 8; ++d0)
; #pragma unroll
;       for (int i = 0; i < 8; ++i) { const float x = bf2f((unsigned)(unsigned short)qr[d0][i]); ss += x * x; }
;     { auto rr = __builtin_amdgcn_permlane32_swap(__float_as_uint(ss), __float_as_uint(ss), false, false); ss = __uint_as_float(rr[0]) + __uint_as_float(rr[1]); }
;     const float rinv = 1.0f / sqrtf(ss * (1.0f / 128.0f) + RMS_EPS);
;     const int t = tpos0 + wid * QBLK + r32;
; #pragma unroll
;     for (int ax = 0; ax < 2; ++ax) { const int pos = ax ? (t & 63) : (t >> 6);
; #pragma unroll
;       for (int q = 0; q < 2; ++q) { const int dl = 4 * ax + q, dh = dl + 2, p0 = q * 16 + 8 * hi;
;         const float* cp_ = rope + pos * 32 + p0; const float* gl = qgain + dl * 16 + 8 * hi; const float* gh = qgain + dh * 16 + 8 * hi;
;         float cs[8], sn[8], lo[8], hv[8];
; #pragma unroll
;         for (int i = 0; i < 8; ++i) { cs[i] = cp_[i]; sn[i] = cp_[4096 + i];
.LBB0_405:
	s_and_b64 vcc, exec, s[4:5]
	s_cbranch_vccz .LBB0_437
	s_cmp_lg_u32 s100, 0
	s_cbranch_scc1 .Lorig_entry
	v_mov_b32_e32 v147, v0
	s_mul_i32 s2, s71, 0x1800
	v_and_b32_e32 v3, 0x60, v147
	v_lshlrev_b32_e32 v5, 3, v147
	v_and_b32_e32 v176, 15, v147
	v_lshrrev_b32_e32 v2, 2, v147
	v_and_or_b32 v3, v5, 24, v3
	v_and_b32_e32 v4, 16, v147
	v_xor_b32_e32 v3, v3, v4
	v_ashrrev_i32_e32 v5, 4, v147
	v_bfe_u32 v146, v147, 2, 2
	v_and_b32_e32 v148, 4, v2
	v_bitop3_b32 v6, v5, v176, 15 bitop3:0x6c
	v_lshlrev_b32_e32 v149, 8, v5
	v_and_b32_e32 v154, 0xfffff0, v5
	v_or_b32_e32 v2, v148, v146
	v_and_b32_e32 v156, 8, v5
	s_mul_hi_u32 s3, s70, 0x1800
	v_lshlrev_b32_e32 v3, 1, v3
	v_or3_b32 v5, v154, v156, v2
	s_add_i32 s3, s3, s2
	s_mul_i32 s2, s70, 0x1800
	v_lshl_or_b32 v30, v5, 8, v3
	v_add_u32_e32 v5, 0x200, v147
	s_add_u32 s2, s22, s2
	v_ashrrev_i32_e32 v5, 4, v5
	s_addc_u32 s3, s88, s3
	s_lshl_b64 s[44:45], s[72:73], 1
	v_lshlrev_b32_e32 v150, 4, v6
	v_bitop3_b32 v6, v5, v176, 15 bitop3:0x6c
	v_lshlrev_b32_e32 v151, 8, v5
	v_and_b32_e32 v153, 0xfffff0, v5
	s_add_u32 s2, s2, s44
	v_ashrrev_i32_e32 v179, 6, v147
	v_and_b32_e32 v155, 8, v5
	s_addc_u32 s3, s3, s45
	v_and_b32_e32 v177, 31, v147
	v_lshlrev_b32_e32 v164, 5, v179
	v_or3_b32 v2, v153, v155, v2
	v_or_b32_e32 v4, v164, v177
	v_lshl_or_b32 v34, v2, 8, v3
	v_mov_b64_e32 v[2:3], s[2:3]
	s_movk_i32 s2, 0x1800
	v_mad_i64_i32 v[2:3], s[2:3], v4, s2, v[2:3]
	v_readfirstlane_b32 s2, v179
	s_lshl_b32 s2, s2, 10
	s_add_i32 s96, s2, 0
	v_or_b32_e32 v162, v150, v149
	s_add_i32 s2, s96, 0x4000
	s_mov_b32 m0, s96
	v_lshlrev_b32_e32 v152, 4, v6
	global_load_lds_dwordx4 v162, s[38:39]
	s_mov_b32 m0, s2
	v_or_b32_e32 v32, v152, v151
	global_load_lds_dwordx4 v30, s[40:41]
	s_add_i32 m0, s96, 0x2000
	v_bfe_u32 v178, v147, 5, 1
	global_load_lds_dwordx4 v32, s[38:39]
	s_add_i32 m0, s96, 0x6000
	s_add_u32 s2, s38, 0x4000
	s_addc_u32 s3, s39, 0
	s_add_u32 s4, s40, 0x4000
	global_load_lds_dwordx4 v34, s[40:41]
	s_addc_u32 s5, s41, 0
	s_add_i32 m0, s96, 0x8000
	s_add_i32 s6, s96, 0xc000
	global_load_lds_dwordx4 v162, s[2:3]
	s_mov_b32 m0, s6
	v_lshlrev_b32_e32 v166, 4, v178
	global_load_lds_dwordx4 v30, s[4:5]
	s_add_i32 m0, s96, 0xa000
	v_mov_b32_e32 v167, v163
	global_load_lds_dwordx4 v32, s[2:3]
	s_add_i32 m0, s96, 0xe000
	v_lshl_add_u64 v[2:3], v[2:3], 0, v[166:167]
	global_load_lds_dwordx4 v34, s[4:5]
	global_load_dwordx4 v[102:105], v[2:3], off
	global_load_dwordx4 v[110:113], v[2:3], off offset:32
	global_load_dwordx4 v[98:101], v[2:3], off offset:64
	global_load_dwordx4 v[106:109], v[2:3], off offset:96
	global_load_dwordx4 v[118:121], v[2:3], off offset:128
	global_load_dwordx4 v[126:129], v[2:3], off offset:160
	global_load_dwordx4 v[114:117], v[2:3], off offset:192
	global_load_dwordx4 v[122:125], v[2:3], off offset:224
	s_cmp_lt_i32 s68, 0
	s_cbranch_scc1 .LBB0_408
	v_lshl_or_b32 v3, s68, 8, v177
	v_lshlrev_b32_e32 v2, 3, v178
	v_add_u32_e32 v26, v3, v164
	v_lshlrev_b32_e32 v44, 2, v2
	v_ashrrev_i32_e32 v2, 1, v26
	v_and_b32_e32 v2, 0xffffffe0, v2
	v_ashrrev_i32_e32 v3, 31, v2
	v_mov_b32_e32 v45, v163
	v_lshl_add_u64 v[2:3], v[2:3], 2, s[16:17]
	v_lshl_add_u64 v[76:77], v[2:3], 0, v[44:45]
	s_mov_b64 s[2:3], 0x4000
	v_lshl_add_u64 v[6:7], v[76:77], 0, s[2:3]
	s_waitcnt lgkmcnt(0)
	global_load_dwordx4 v[130:133], v44, s[14:15] offset:16
	global_load_dwordx4 v[14:17], v44, s[14:15] offset:144
	global_load_dwordx4 v[2:5], v[76:77], off offset:16
	s_nop 0
	global_load_dwordx4 v[6:9], v[6:7], off offset:16
	s_nop 0
	global_load_dwordx4 v[22:25], v44, s[14:15]
	global_load_dwordx4 v[18:21], v44, s[14:15] offset:128
	s_waitcnt vmcnt(0)
	v_lshlrev_b32_e32 v38, 16, v129
	v_and_b32_e32 v36, 0xffff0000, v129
	v_lshlrev_b32_e32 v129, 16, v102
	v_lshlrev_b32_e32 v39, 16, v125
	v_and_b32_e32 v37, 0xffff0000, v125
	v_lshlrev_b32_e32 v49, 16, v123
	v_lshlrev_b32_e32 v48, 16, v127
	v_and_b32_e32 v47, 0xffff0000, v123
	v_and_b32_e32 v46, 0xffff0000, v127
	v_lshlrev_b32_e32 v123, 16, v99
	v_and_b32_e32 v127, 0xffff0000, v99
	v_and_b32_e32 v99, 0xffff0000, v102
	v_lshlrev_b32_e32 v53, 16, v122
	v_and_b32_e32 v51, 0xffff0000, v122
	v_lshlrev_b32_e32 v122, 16, v103
	v_lshlrev_b32_e32 v52, 16, v126
	v_and_b32_e32 v50, 0xffff0000, v126
	v_and_b32_e32 v126, 0xffff0000, v103
	v_lshlrev_b32_e32 v90, 16, v111
	v_and_b32_e32 v88, 0xffff0000, v111
	v_lshlrev_b32_e32 v92, 16, v110
	v_and_b32_e32 v94, 0xffff0000, v110
	v_lshlrev_b32_e32 v111, 16, v100
	v_lshlrev_b32_e32 v110, 16, v104
	v_lshlrev_b32_e32 v65, 16, v116
	v_and_b32_e32 v63, 0xffff0000, v116
	v_lshlrev_b32_e32 v73, 16, v114
	v_and_b32_e32 v71, 0xffff0000, v114
	v_lshlrev_b32_e32 v114, 16, v105
	v_and_b32_e32 v116, 0xffff0000, v105
	v_and_b32_e32 v105, 0xffff0000, v100
	v_and_b32_e32 v104, 0xffff0000, v104
	v_lshlrev_b32_e32 v69, 16, v115
	v_and_b32_e32 v67, 0xffff0000, v115
	v_lshlrev_b32_e32 v115, 16, v101
	v_lshlrev_b32_e32 v61, 16, v117
	v_and_b32_e32 v55, 0xffff0000, v117
	v_and_b32_e32 v117, 0xffff0000, v101
	v_lshlrev_b32_e32 v93, 16, v106
	v_and_b32_e32 v95, 0xffff0000, v106
	v_lshlrev_b32_e32 v91, 16, v107
	v_and_b32_e32 v89, 0xffff0000, v107
	v_lshlrev_b32_e32 v87, 16, v108
	v_lshlrev_b32_e32 v86, 16, v112
	v_and_b32_e32 v85, 0xffff0000, v108
	v_and_b32_e32 v84, 0xffff0000, v112
	v_lshlrev_b32_e32 v83, 16, v109
	v_lshlrev_b32_e32 v82, 16, v113
	v_and_b32_e32 v81, 0xffff0000, v109
	v_and_b32_e32 v80, 0xffff0000, v113
	v_lshlrev_b32_e32 v42, 16, v128
	v_and_b32_e32 v40, 0xffff0000, v128
	v_lshlrev_b32_e32 v128, 16, v98
	v_and_b32_e32 v98, 0xffff0000, v98
	s_movk_i32 s4, 0x4000
	v_lshlrev_b32_e32 v26, 7, v26
	v_add_co_u32_e32 v78, vcc, s4, v76
; __device__ __forceinline__ void attn_dma_body(const bf16_t* __restrict__ Qb, int ldq, int tpos0, const float* __restrict__ rope, const float* __restrict__ qgain, ...
;     ...
;     float ss = 0.f;
; #pragma unroll
;     for (int d0 = 0; d0 < 8; ++d0)
; #pragma unroll
;       for (int i = 0; i < 8; ++i) { const float x = bf2f((unsigned)(unsigned short)qr[d0][i]); ss += x * x; }
;     { auto rr = __builtin_amdgcn_permlane32_swap(__float_as_uint(ss), __float_as_uint(ss), false, false); ss = __uint_as_float(rr[0]) + __uint_as_float(rr[1]); }
;     const float rinv = 1.0f / sqrtf(ss * (1.0f / 128.0f) + RMS_EPS);
;     const int t = tpos0 + wid * QBLK + r32;
	v_mov_b32_e32 v27, v163
	v_and_b32_e32 v26, 0x1f80, v26
	v_addc_co_u32_e32 v79, vcc, 0, v77, vcc
	v_lshl_add_u64 v[26:27], s[16:17], 0, v[26:27]
	global_load_dwordx4 v[10:13], v[78:79], off
	v_lshl_add_u64 v[58:59], v[26:27], 0, v[44:45]
	global_load_dwordx4 v[26:29], v[76:77], off
	v_lshlrev_b32_e32 v72, 16, v118
	v_and_b32_e32 v70, 0xffff0000, v118
	v_lshlrev_b32_e32 v68, 16, v119
	v_and_b32_e32 v66, 0xffff0000, v119
	v_lshlrev_b32_e32 v64, 16, v120
	v_and_b32_e32 v62, 0xffff0000, v120
	v_lshlrev_b32_e32 v60, 16, v121
	v_and_b32_e32 v54, 0xffff0000, v121
	v_lshlrev_b32_e32 v43, 16, v124
	v_and_b32_e32 v41, 0xffff0000, v124
	v_mov_b32_e32 v134, v37
	v_mov_b32_e32 v135, v39
	v_lshl_add_u64 v[74:75], v[58:59], 0, s[2:3]
	v_mov_b32_e32 v125, v20
	v_mul_f32_e32 v20, v129, v129
	v_fmac_f32_e32 v20, v99, v99
	v_pk_fma_f32 v[102:103], v[122:123], v[122:123], v[20:21] op_sel_hi:[1,1,0]
	v_mul_f32_e32 v20, v123, v123
	v_pk_fma_f32 v[102:103], v[126:127], v[126:127], v[102:103]
	s_mov_b32 s2, 0xf800000
	v_pk_fma_f32 v[102:103], v[110:111], v[110:111], v[102:103]
	v_mov_b32_e32 v124, v24
	v_pk_fma_f32 v[102:103], v[104:105], v[104:105], v[102:103]
	v_mov_b32_e32 v120, v130
	v_pk_fma_f32 v[102:103], v[114:115], v[114:115], v[102:103]
	v_mov_b32_e32 v121, v14
	v_pk_fma_f32 v[102:103], v[116:117], v[116:117], v[102:103]
	v_mov_b32_e32 v14, v131
	v_pk_fma_f32 v[102:103], v[92:93], v[92:93], v[102:103]
	v_mov_b32_e32 v118, v132
	v_pk_fma_f32 v[102:103], v[94:95], v[94:95], v[102:103]
	v_mov_b32_e32 v119, v16
	v_pk_fma_f32 v[102:103], v[90:91], v[90:91], v[102:103]
	v_mov_b32_e32 v16, v133
	v_pk_fma_f32 v[102:103], v[88:89], v[88:89], v[102:103]
	v_mov_b32_e32 v106, v6
	v_pk_fma_f32 v[102:103], v[86:87], v[86:87], v[102:103]
	v_mov_b32_e32 v107, v2
	v_pk_fma_f32 v[102:103], v[84:85], v[84:85], v[102:103]
	v_lshl_add_u64 v[96:97], v[76:77], 0, s[24:25]
	v_pk_fma_f32 v[102:103], v[82:83], v[82:83], v[102:103]
	v_mov_b32_e32 v112, v8
	v_pk_fma_f32 v[102:103], v[80:81], v[80:81], v[102:103]
	v_mov_b32_e32 v113, v4
	v_pk_fma_f32 v[102:103], v[128:129], v[128:129], v[102:103]
	v_mov_b32_e32 v108, v9
	v_pk_fma_f32 v[102:103], v[98:99], v[98:99], v[102:103]
	v_mov_b32_e32 v109, v5
	v_pk_add_f32 v[102:103], v[20:21], v[102:103] op_sel_hi:[0,1]
	v_mul_f32_e32 v20, v127, v127
	v_pk_add_f32 v[102:103], v[20:21], v[102:103] op_sel_hi:[0,1]
	v_mul_f32_e32 v20, v111, v111
	v_pk_add_f32 v[102:103], v[20:21], v[102:103] op_sel_hi:[0,1]
	v_mul_f32_e32 v20, v105, v105
	v_pk_add_f32 v[102:103], v[20:21], v[102:103] op_sel_hi:[0,1]
	v_mul_f32_e32 v20, v115, v115
	v_pk_add_f32 v[102:103], v[20:21], v[102:103] op_sel_hi:[0,1]
	v_mul_f32_e32 v20, v117, v117
	v_pk_add_f32 v[102:103], v[20:21], v[102:103] op_sel_hi:[0,1]
	v_mul_f32_e32 v20, v93, v93
	v_pk_add_f32 v[102:103], v[20:21], v[102:103] op_sel_hi:[0,1]
	v_mul_f32_e32 v20, v95, v95
	v_pk_add_f32 v[102:103], v[20:21], v[102:103] op_sel_hi:[0,1]
	v_mul_f32_e32 v20, v91, v91
	v_pk_add_f32 v[102:103], v[20:21], v[102:103] op_sel_hi:[0,1]
	v_mul_f32_e32 v20, v89, v89
	v_pk_add_f32 v[102:103], v[20:21], v[102:103] op_sel_hi:[0,1]
	v_mul_f32_e32 v20, v87, v87
	v_pk_add_f32 v[102:103], v[20:21], v[102:103] op_sel_hi:[0,1]
	v_mul_f32_e32 v20, v85, v85
	v_pk_add_f32 v[102:103], v[20:21], v[102:103] op_sel_hi:[0,1]
	v_mul_f32_e32 v20, v83, v83
	v_pk_add_f32 v[102:103], v[20:21], v[102:103] op_sel_hi:[0,1]
	v_mul_f32_e32 v20, v81, v81
	v_pk_add_f32 v[102:103], v[20:21], v[102:103] op_sel_hi:[0,1]
	v_pk_fma_f32 v[102:103], v[72:73], v[72:73], v[102:103]
	v_mul_f32_e32 v20, v73, v73
	v_pk_fma_f32 v[102:103], v[70:71], v[70:71], v[102:103]
	s_waitcnt vmcnt(1)
	v_mov_b32_e32 v100, v12
	v_pk_fma_f32 v[102:103], v[68:69], v[68:69], v[102:103]
	s_waitcnt vmcnt(0)
	v_mov_b32_e32 v101, v28
	v_pk_fma_f32 v[102:103], v[66:67], v[66:67], v[102:103]
	v_lshl_add_u64 v[56:57], v[58:59], 0, s[24:25]
	v_pk_fma_f32 v[102:103], v[64:65], v[64:65], v[102:103]
	s_nop 0
	v_pk_fma_f32 v[102:103], v[62:63], v[62:63], v[102:103]
	s_nop 0
	v_pk_fma_f32 v[102:103], v[60:61], v[60:61], v[102:103]
	s_nop 0
	v_pk_fma_f32 v[102:103], v[54:55], v[54:55], v[102:103]
	s_nop 0
	v_pk_fma_f32 v[102:103], v[52:53], v[52:53], v[102:103]
	s_nop 0
	v_pk_fma_f32 v[102:103], v[50:51], v[50:51], v[102:103]
	s_nop 0
	v_pk_fma_f32 v[102:103], v[48:49], v[48:49], v[102:103]
	s_nop 0
	v_pk_fma_f32 v[102:103], v[46:47], v[46:47], v[102:103]
	s_nop 0
	v_pk_fma_f32 v[102:103], v[42:43], v[42:43], v[102:103]
	s_nop 0
	v_pk_fma_f32 v[102:103], v[40:41], v[40:41], v[102:103]
	s_nop 0
	v_pk_fma_f32 v[102:103], v[38:39], v[38:39], v[102:103]
	s_nop 0
	v_pk_fma_f32 v[102:103], v[36:37], v[36:37], v[102:103]
	s_nop 0
	v_pk_add_f32 v[102:103], v[20:21], v[102:103] op_sel_hi:[0,1]
	v_mul_f32_e32 v20, v71, v71
	v_pk_add_f32 v[102:103], v[20:21], v[102:103] op_sel_hi:[0,1]
	v_mul_f32_e32 v20, v69, v69
	v_pk_add_f32 v[102:103], v[20:21], v[102:103] op_sel_hi:[0,1]
	v_mul_f32_e32 v20, v67, v67
	v_pk_add_f32 v[102:103], v[20:21], v[102:103] op_sel_hi:[0,1]
	v_mul_f32_e32 v20, v65, v65
	v_pk_add_f32 v[102:103], v[20:21], v[102:103] op_sel_hi:[0,1]
	v_mul_f32_e32 v20, v63, v63
	v_pk_add_f32 v[102:103], v[20:21], v[102:103] op_sel_hi:[0,1]
	v_mul_f32_e32 v20, v61, v61
	v_pk_add_f32 v[102:103], v[20:21], v[102:103] op_sel_hi:[0,1]
	v_mul_f32_e32 v20, v55, v55
	v_pk_add_f32 v[102:103], v[20:21], v[102:103] op_sel_hi:[0,1]
	v_mul_f32_e32 v20, v53, v53
	v_pk_add_f32 v[102:103], v[20:21], v[102:103] op_sel_hi:[0,1]
	v_mul_f32_e32 v20, v51, v51
	v_pk_add_f32 v[102:103], v[20:21], v[102:103] op_sel_hi:[0,1]
	v_mul_f32_e32 v20, v49, v49
	v_pk_add_f32 v[102:103], v[20:21], v[102:103] op_sel_hi:[0,1]
; __device__ __forceinline__ unsigned pk2(float lo, float hi) { unsigned r; asm("v_cvt_pk_bf16_f32 %0, %1, %2" : "=v"(r) : "v"(lo), "v"(hi)); return r; }
; __device__ __forceinline__ void attn_dma_body(const bf16_t* __restrict__ Qb, int ldq, int tpos0, const float* __restrict__ rope, const float* __restrict__ qgain, ...
;     ...
;     { auto rr = __builtin_amdgcn_permlane32_swap(__float_as_uint(ss), __float_as_uint(ss), false, false); ss = __uint_as_float(rr[0]) + __uint_as_float(rr[1]); }
;     const float rinv = 1.0f / sqrtf(ss * (1.0f / 128.0f) + RMS_EPS);
;     const int t = tpos0 + wid * QBLK + r32;
; #pragma unroll
;     for (int ax = 0; ax < 2; ++ax) { const int pos = ax ? (t & 63) : (t >> 6);
; #pragma unroll
;       for (int q = 0; q < 2; ++q) { const int dl = 4 * ax + q, dh = dl + 2, p0 = q * 16 + 8 * hi;
;         const float* cp_ = rope + pos * 32 + p0; const float* gl = qgain + dl * 16 + 8 * hi; const float* gh = qgain + dh * 16 + 8 * hi;
;         float cs[8], sn[8], lo[8], hv[8];
; #pragma unroll
;         for (int i = 0; i < 8; ++i) { cs[i] = cp_[i]; sn[i] = cp_[4096 + i];
;           lo[i] = bf2f((unsigned)(unsigned short)qr[dl][i]) * rinv * gl[i]; hv[i] = bf2f((unsigned)(unsigned short)qr[dh][i]) * rinv * gh[i]; }
;         u32x4 wl, wh;
; #pragma unroll
;         for (int i = 0; i < 4; ++i) { const float l0 = lo[2 * i] * cs[2 * i] - hv[2 * i] * sn[2 * i], l1 = lo[2 * i + 1] * cs[2 * i + 1] - hv[2 * i + 1] * sn[2 * i + 1];
;           const float h0 = hv[2 * i] * cs[2 * i] + lo[2 * i] * sn[2 * i], h1 = hv[2 * i + 1] * cs[2 * i + 1] + lo[2 * i + 1] * sn[2 * i + 1];
;           wl[i] = pk2(l0, l1); wh[i] = pk2(h0, h1); }
;         qr[dl] = *reinterpret_cast<bf16x8*>(&wl); qr[dh] = *reinterpret_cast<bf16x8*>(&wh); } } }
	v_mul_f32_e32 v20, v47, v47
	v_pk_add_f32 v[102:103], v[20:21], v[102:103] op_sel_hi:[0,1]
	v_mul_f32_e32 v20, v43, v43
	v_pk_add_f32 v[102:103], v[20:21], v[102:103] op_sel_hi:[0,1]
	v_mul_f32_e32 v20, v41, v41
	v_pk_add_f32 v[102:103], v[20:21], v[102:103] op_sel_hi:[0,1]
	v_mul_f32_e32 v20, v39, v39
	v_pk_add_f32 v[102:103], v[20:21], v[102:103] op_sel_hi:[0,1]
	v_pk_fma_f32 v[102:103], v[134:135], v[134:135], v[102:103]
	global_load_dwordx4 v[130:133], v44, s[14:15] offset:80
	global_load_dwordx4 v[134:137], v44, s[14:15] offset:64
	global_load_dwordx4 v[138:141], v44, s[14:15] offset:208
	global_load_dwordx4 v[142:145], v44, s[14:15] offset:192
	v_mov_b32_e32 v20, v102
	s_nop 1
	v_permlane32_swap_b32_e32 v102, v20
	v_add_f32_e32 v20, v102, v20
	v_fmamk_f32 v20, v20, 0x3c000000, v1
	v_mul_f32_e32 v24, 0x4f800000, v20
	v_cmp_gt_f32_e32 vcc, s2, v20
	v_mov_b32_e32 v102, v26
	v_mov_b32_e32 v103, v10
	v_cndmask_b32_e32 v31, v20, v24, vcc
	v_sqrt_f32_e32 v33, v31
	v_mov_b32_e32 v24, v18
	v_mov_b32_e32 v20, v25
	v_add_u32_e32 v18, -1, v33
	v_fma_f32 v25, -v18, v33, v31
	v_cmp_ge_f32_e64 s[2:3], 0, v25
	v_add_u32_e32 v25, 1, v33
	s_nop 0
	v_cndmask_b32_e64 v18, v33, v18, s[2:3]
	v_fma_f32 v33, -v25, v33, v31
	v_cmp_lt_f32_e64 s[2:3], 0, v33
	s_nop 1
	v_cndmask_b32_e64 v18, v18, v25, s[2:3]
	v_mul_f32_e32 v25, 0x37800000, v18
	v_cndmask_b32_e32 v18, v18, v25, vcc
	v_cmp_class_f32_e32 vcc, v31, v174
	v_mov_b32_e32 v25, v22
	s_nop 0
	v_cndmask_b32_e32 v18, v18, v31, vcc
	v_div_scale_f32 v31, s[2:3], v18, v18, 1.0
	v_rcp_f32_e32 v33, v31
	s_nop 0
	v_fma_f32 v22, -v31, v33, 1.0
	v_fmac_f32_e32 v33, v22, v33
	v_div_scale_f32 v22, vcc, 1.0, v18, 1.0
	v_mul_f32_e32 v35, v22, v33
	v_fma_f32 v45, -v31, v35, v22
	v_fmac_f32_e32 v35, v45, v33
	v_fma_f32 v22, -v31, v35, v22
	v_div_fmas_f32 v22, v22, v33, v35
	v_div_fixup_f32 v18, v22, v18, 1.0
	v_mul_f32_e32 v18, 0x3e0293ee, v18
	v_pk_mul_f32 v[98:99], v[18:19], v[98:99] op_sel_hi:[0,1]
	v_mov_b32_e32 v22, v19
	v_pk_mul_f32 v[98:99], v[98:99], v[22:23]
	v_pk_mul_f32 v[22:23], v[18:19], v[122:123] op_sel_hi:[0,1]
	v_pk_mul_f32 v[122:123], v[22:23], v[124:125]
	v_pk_mul_f32 v[22:23], v[18:19], v[126:127] op_sel_hi:[0,1]
	v_pk_mul_f32 v[124:125], v[22:23], v[20:21]
	v_pk_mul_f32 v[20:21], v[18:19], v[110:111] op_sel_hi:[0,1]
	v_pk_mul_f32 v[110:111], v[20:21], v[120:121]
	v_pk_mul_f32 v[20:21], v[18:19], v[104:105] op_sel_hi:[0,1]
	v_pk_mul_f32 v[104:105], v[20:21], v[14:15]
	v_pk_mul_f32 v[14:15], v[18:19], v[114:115] op_sel_hi:[0,1]
	v_pk_mul_f32 v[128:129], v[18:19], v[128:129] op_sel_hi:[0,1]
	v_pk_mul_f32 v[114:115], v[14:15], v[118:119]
	v_pk_mul_f32 v[14:15], v[18:19], v[116:117] op_sel_hi:[0,1]
	v_pk_mul_f32 v[24:25], v[24:25], v[128:129]
	v_pk_mul_f32 v[116:117], v[14:15], v[16:17]
	v_mov_b32_e32 v14, v10
	v_mov_b32_e32 v15, v26
	v_pk_mul_f32 v[14:15], v[14:15], v[24:25]
	v_mov_b32_e32 v26, v11
	v_sub_f32_e32 v19, v15, v14
	v_pk_mul_f32 v[14:15], v[26:27], v[98:99]
	v_mov_b32_e32 v10, v27
	v_sub_f32_e32 v31, v15, v14
	v_pk_mul_f32 v[14:15], v[102:103], v[24:25]
	v_pk_mul_f32 v[10:11], v[10:11], v[98:99]
	v_add_f32_e32 v33, v14, v15
	global_load_dwordx4 v[14:17], v[76:77], off offset:80
	global_load_dwordx4 v[20:23], v[76:77], off offset:64
	global_load_dwordx4 v[24:27], v[78:79], off offset:64
	v_add_f32_e32 v10, v10, v11
	v_cvt_pk_bf16_f32 v98, v33, v10
	v_mov_b32_e32 v10, v28
	v_mov_b32_e32 v11, v12
	v_pk_mul_f32 v[10:11], v[10:11], v[122:123]
	v_mov_b32_e32 v12, v29
	v_cvt_pk_bf16_f32 v102, v19, v31
	v_sub_f32_e32 v19, v10, v11
	v_pk_mul_f32 v[10:11], v[12:13], v[124:125]
	v_mov_b32_e32 v28, v13
	v_sub_f32_e32 v12, v10, v11
	v_pk_mul_f32 v[10:11], v[100:101], v[122:123]
	v_cvt_pk_bf16_f32 v103, v19, v12
	s_waitcnt vmcnt(3)
	v_mov_b32_e32 v13, v144
	v_add_f32_e32 v31, v10, v11
	v_pk_mul_f32 v[10:11], v[28:29], v[124:125]
	v_mov_b32_e32 v144, v137
	v_add_f32_e32 v10, v10, v11
	v_cvt_pk_bf16_f32 v99, v31, v10
	v_mov_b32_e32 v10, v2
	v_mov_b32_e32 v11, v6
	v_pk_mul_f32 v[10:11], v[10:11], v[110:111]
	v_mov_b32_e32 v6, v3
	v_mov_b32_e32 v2, v7
	v_sub_f32_e32 v12, v10, v11
	v_pk_mul_f32 v[10:11], v[6:7], v[104:105]
	v_pk_mul_f32 v[2:3], v[2:3], v[104:105]
	v_sub_f32_e32 v6, v10, v11
	v_pk_mul_f32 v[10:11], v[106:107], v[110:111]
	v_add_f32_e32 v2, v2, v3
	v_add_f32_e32 v10, v10, v11
	v_cvt_pk_bf16_f32 v100, v10, v2
	v_mov_b32_e32 v2, v4
	v_mov_b32_e32 v3, v8
	v_pk_mul_f32 v[2:3], v[2:3], v[114:115]
	v_mov_b32_e32 v8, v5
	v_cvt_pk_bf16_f32 v104, v12, v6
	v_sub_f32_e32 v4, v2, v3
	v_pk_mul_f32 v[2:3], v[8:9], v[116:117]
	global_load_dwordx4 v[6:9], v[96:97], off offset:16
	v_sub_f32_e32 v5, v2, v3
	v_pk_mul_f32 v[2:3], v[112:113], v[114:115]
	v_mov_b32_e32 v12, v136
	v_add_f32_e32 v10, v2, v3
	v_pk_mul_f32 v[2:3], v[108:109], v[116:117]
	v_cvt_pk_bf16_f32 v105, v4, v5
	v_mov_b32_e32 v4, v134
	v_add_f32_e32 v2, v2, v3
	v_cvt_pk_bf16_f32 v101, v10, v2
	v_pk_mul_f32 v[10:11], v[18:19], v[90:91] op_sel_hi:[0,1]
	v_pk_mul_f32 v[28:29], v[10:11], v[12:13]
	v_pk_mul_f32 v[10:11], v[18:19], v[88:89] op_sel_hi:[0,1]
	v_pk_mul_f32 v[96:97], v[10:11], v[144:145]
	v_pk_mul_f32 v[10:11], v[18:19], v[86:87] op_sel_hi:[0,1]
	v_mov_b32_e32 v12, v130
	v_mov_b32_e32 v13, v138
	v_pk_mul_f32 v[2:3], v[18:19], v[92:93] op_sel_hi:[0,1]
	v_mov_b32_e32 v5, v142
	v_pk_mul_f32 v[108:109], v[10:11], v[12:13]
	v_mov_b32_e32 v13, v140
	v_pk_mul_f32 v[88:89], v[18:19], v[80:81] op_sel_hi:[0,1]
	v_mov_b32_e32 v140, v133
	v_pk_mul_f32 v[2:3], v[2:3], v[4:5]
	v_pk_mul_f32 v[116:117], v[88:89], v[140:141]
	v_pk_mul_f32 v[4:5], v[18:19], v[94:95] op_sel_hi:[0,1]
	v_mov_b32_e32 v142, v135
	v_pk_mul_f32 v[10:11], v[18:19], v[84:85] op_sel_hi:[0,1]
	v_mov_b32_e32 v138, v131
	v_pk_mul_f32 v[4:5], v[4:5], v[142:143]
	v_pk_mul_f32 v[112:113], v[10:11], v[138:139]
	v_pk_mul_f32 v[10:11], v[18:19], v[82:83] op_sel_hi:[0,1]
	v_mov_b32_e32 v12, v132
	v_pk_mul_f32 v[114:115], v[10:11], v[12:13]
	global_load_dwordx4 v[10:13], v44, s[14:15] offset:272
	global_load_dwordx4 v[76:79], v44, s[14:15] offset:256
	global_load_dwordx4 v[80:83], v44, s[14:15] offset:400
	global_load_dwordx4 v[84:87], v44, s[14:15] offset:384
	v_add_co_u32_e32 v118, vcc, s4, v58
	s_waitcnt vmcnt(6)
; __device__ __forceinline__ unsigned pk2(float lo, float hi) { unsigned r; asm("v_cvt_pk_bf16_f32 %0, %1, %2" : "=v"(r) : "v"(lo), "v"(hi)); return r; }
; __device__ __forceinline__ void attn_dma_body(const bf16_t* __restrict__ Qb, int ldq, int tpos0, const float* __restrict__ rope, const float* __restrict__ qgain, ...
;     ...
; #pragma unroll
;     for (int ax = 0; ax < 2; ++ax) { const int pos = ax ? (t & 63) : (t >> 6);
; #pragma unroll
;       for (int q = 0; q < 2; ++q) { const int dl = 4 * ax + q, dh = dl + 2, p0 = q * 16 + 8 * hi;
;         const float* cp_ = rope + pos * 32 + p0; const float* gl = qgain + dl * 16 + 8 * hi; const float* gh = qgain + dh * 16 + 8 * hi;
;         float cs[8], sn[8], lo[8], hv[8];
; #pragma unroll
;         for (int i = 0; i < 8; ++i) { cs[i] = cp_[i]; sn[i] = cp_[4096 + i];
;           lo[i] = bf2f((unsigned)(unsigned short)qr[dl][i]) * rinv * gl[i]; hv[i] = bf2f((unsigned)(unsigned short)qr[dh][i]) * rinv * gh[i]; }
;         u32x4 wl, wh;
; #pragma unroll
;         for (int i = 0; i < 4; ++i) { const float l0 = lo[2 * i] * cs[2 * i] - hv[2 * i] * sn[2 * i], l1 = lo[2 * i + 1] * cs[2 * i + 1] - hv[2 * i + 1] * sn[2 * i + 1];
;           const float h0 = hv[2 * i] * cs[2 * i] + lo[2 * i] * sn[2 * i], h1 = hv[2 * i + 1] * cs[2 * i + 1] + lo[2 * i + 1] * sn[2 * i + 1];
;           wl[i] = pk2(l0, l1); wh[i] = pk2(h0, h1); }
;         qr[dl] = *reinterpret_cast<bf16x8*>(&wl); qr[dh] = *reinterpret_cast<bf16x8*>(&wh); } } }
	v_mov_b32_e32 v88, v20
	s_waitcnt vmcnt(5)
	v_mov_b32_e32 v89, v24
	v_pk_mul_f32 v[88:89], v[88:89], v[2:3]
	v_addc_co_u32_e32 v119, vcc, 0, v59, vcc
	v_sub_f32_e32 v19, v88, v89
	v_mov_b32_e32 v88, v21
	v_mov_b32_e32 v89, v25
	v_pk_mul_f32 v[88:89], v[88:89], v[4:5]
	s_nop 0
	v_sub_f32_e32 v31, v88, v89
	v_mov_b32_e32 v88, v24
	v_mov_b32_e32 v89, v20
	v_pk_mul_f32 v[2:3], v[88:89], v[2:3]
	v_mov_b32_e32 v20, v25
	v_add_f32_e32 v24, v2, v3
	v_pk_mul_f32 v[2:3], v[20:21], v[4:5]
	v_cvt_pk_bf16_f32 v110, v19, v31
	s_nop 0
	v_add_f32_e32 v2, v2, v3
	v_cvt_pk_bf16_f32 v106, v24, v2
	v_mov_b32_e32 v2, v22
	v_mov_b32_e32 v3, v26
	v_pk_mul_f32 v[2:3], v[2:3], v[28:29]
	s_nop 0
	v_sub_f32_e32 v19, v2, v3
	v_mov_b32_e32 v2, v23
	v_mov_b32_e32 v3, v27
	v_pk_mul_f32 v[20:21], v[2:3], v[96:97]
	global_load_dwordx4 v[2:5], v[58:59], off offset:16
	global_load_dwordx4 v[88:91], v[58:59], off
	global_load_dwordx4 v[92:95], v[118:119], off
	v_sub_f32_e32 v24, v20, v21
	v_mov_b32_e32 v20, v26
	v_mov_b32_e32 v21, v22
	v_pk_mul_f32 v[20:21], v[20:21], v[28:29]
	v_mov_b32_e32 v22, v27
	v_add_f32_e32 v25, v20, v21
	v_pk_mul_f32 v[20:21], v[22:23], v[96:97]
	v_cvt_pk_bf16_f32 v111, v19, v24
	s_nop 0
	v_add_f32_e32 v20, v20, v21
	v_cvt_pk_bf16_f32 v107, v25, v20
	v_mov_b32_e32 v20, v14
	s_waitcnt vmcnt(7)
	v_mov_b32_e32 v21, v6
	v_pk_mul_f32 v[20:21], v[20:21], v[108:109]
	s_nop 0
	v_sub_f32_e32 v19, v20, v21
	v_mov_b32_e32 v20, v15
	v_mov_b32_e32 v21, v7
	v_pk_mul_f32 v[20:21], v[20:21], v[112:113]
	s_nop 0
	v_sub_f32_e32 v22, v20, v21
	v_mov_b32_e32 v21, v14
	v_mov_b32_e32 v14, v7
	v_mov_b32_e32 v20, v6
	v_pk_mul_f32 v[6:7], v[14:15], v[112:113]
	v_pk_mul_f32 v[20:21], v[20:21], v[108:109]
	v_add_f32_e32 v6, v6, v7
	v_add_f32_e32 v20, v20, v21
	v_cvt_pk_bf16_f32 v108, v20, v6
	v_mov_b32_e32 v6, v16
	v_mov_b32_e32 v7, v8
	v_cvt_pk_bf16_f32 v112, v19, v22
	v_pk_mul_f32 v[6:7], v[6:7], v[114:115]
	global_load_dwordx4 v[20:23], v[74:75], off offset:16
	v_sub_f32_e32 v14, v6, v7
	v_mov_b32_e32 v6, v17
	v_mov_b32_e32 v7, v9
	v_pk_mul_f32 v[6:7], v[6:7], v[116:117]
	s_nop 0
	v_sub_f32_e32 v15, v6, v7
	v_mov_b32_e32 v6, v8
	v_mov_b32_e32 v7, v16
	v_pk_mul_f32 v[6:7], v[6:7], v[114:115]
	v_mov_b32_e32 v16, v9
	v_add_f32_e32 v8, v6, v7
	v_pk_mul_f32 v[6:7], v[16:17], v[116:117]
	s_waitcnt vmcnt(4)
	v_mov_b32_e32 v9, v84
	v_add_f32_e32 v6, v6, v7
	v_cvt_pk_bf16_f32 v109, v8, v6
	v_pk_mul_f32 v[6:7], v[18:19], v[72:73] op_sel_hi:[0,1]
	v_mov_b32_e32 v8, v76
	v_pk_mul_f32 v[28:29], v[6:7], v[8:9]
	v_pk_mul_f32 v[6:7], v[18:19], v[70:71] op_sel_hi:[0,1]
	v_mov_b32_e32 v84, v77
	v_pk_mul_f32 v[70:71], v[6:7], v[84:85]
	v_pk_mul_f32 v[6:7], v[18:19], v[68:69] op_sel_hi:[0,1]
	v_mov_b32_e32 v8, v78
	v_mov_b32_e32 v9, v86
	v_pk_mul_f32 v[72:73], v[6:7], v[8:9]
	v_pk_mul_f32 v[6:7], v[18:19], v[66:67] op_sel_hi:[0,1]
	v_mov_b32_e32 v86, v79
	v_pk_mul_f32 v[74:75], v[6:7], v[86:87]
	v_pk_mul_f32 v[6:7], v[18:19], v[64:65] op_sel_hi:[0,1]
	v_mov_b32_e32 v8, v10
	v_mov_b32_e32 v9, v80
	v_pk_mul_f32 v[76:77], v[6:7], v[8:9]
	v_pk_mul_f32 v[6:7], v[18:19], v[62:63] op_sel_hi:[0,1]
	v_mov_b32_e32 v80, v11
	v_pk_mul_f32 v[10:11], v[18:19], v[60:61] op_sel_hi:[0,1]
	v_mov_b32_e32 v64, v12
	v_mov_b32_e32 v65, v82
	v_cvt_pk_bf16_f32 v113, v14, v15
	v_pk_mul_f32 v[78:79], v[6:7], v[80:81]
	global_load_dwordx4 v[6:9], v44, s[14:15] offset:336
	global_load_dwordx4 v[14:17], v44, s[14:15] offset:320
	global_load_dwordx4 v[24:27], v44, s[14:15] offset:464
	global_load_dwordx4 v[60:63], v44, s[14:15] offset:448
	v_pk_mul_f32 v[44:45], v[10:11], v[64:65]
	v_pk_mul_f32 v[10:11], v[18:19], v[54:55] op_sel_hi:[0,1]
	v_mov_b32_e32 v82, v13
	v_pk_mul_f32 v[80:81], v[10:11], v[82:83]
	s_waitcnt vmcnt(6)
	v_mov_b32_e32 v54, v88
	s_waitcnt vmcnt(5)
	v_mov_b32_e32 v55, v92
	v_pk_mul_f32 v[54:55], v[54:55], v[28:29]
	global_load_dwordx4 v[10:13], v[118:119], off offset:64
	v_sub_f32_e32 v19, v54, v55
	v_mov_b32_e32 v54, v89
	v_mov_b32_e32 v55, v93
	v_pk_mul_f32 v[54:55], v[54:55], v[70:71]
	s_nop 0
	v_sub_f32_e32 v31, v54, v55
	v_mov_b32_e32 v54, v92
	v_mov_b32_e32 v55, v88
	v_pk_mul_f32 v[28:29], v[54:55], v[28:29]
	v_mov_b32_e32 v88, v93
	v_add_f32_e32 v33, v28, v29
	v_pk_mul_f32 v[28:29], v[88:89], v[70:71]
	global_load_dwordx4 v[64:67], v[58:59], off offset:80
	global_load_dwordx4 v[68:71], v[58:59], off offset:64
	v_add_f32_e32 v28, v28, v29
	global_load_dwordx4 v[54:57], v[56:57], off offset:16
	v_cvt_pk_bf16_f32 v114, v33, v28
	v_mov_b32_e32 v28, v90
	v_mov_b32_e32 v29, v94
	v_pk_mul_f32 v[28:29], v[28:29], v[72:73]
	v_cvt_pk_bf16_f32 v118, v19, v31
	s_nop 0
	v_sub_f32_e32 v19, v28, v29
	v_mov_b32_e32 v28, v91
	v_mov_b32_e32 v29, v95
	v_pk_mul_f32 v[28:29], v[28:29], v[74:75]
	s_nop 0
	v_sub_f32_e32 v31, v28, v29
	v_mov_b32_e32 v28, v94
	v_mov_b32_e32 v29, v90
	v_pk_mul_f32 v[28:29], v[28:29], v[72:73]
	v_mov_b32_e32 v90, v95
	v_add_f32_e32 v33, v28, v29
	v_pk_mul_f32 v[28:29], v[90:91], v[74:75]
	v_cvt_pk_bf16_f32 v119, v19, v31
	s_nop 0
	v_add_f32_e32 v28, v28, v29
	v_cvt_pk_bf16_f32 v115, v33, v28
	v_mov_b32_e32 v28, v2
	s_waitcnt vmcnt(8)
; __device__ __forceinline__ unsigned pk2(float lo, float hi) { unsigned r; asm("v_cvt_pk_bf16_f32 %0, %1, %2" : "=v"(r) : "v"(lo), "v"(hi)); return r; }
; __device__ __forceinline__ void attn_dma_body(const bf16_t* __restrict__ Qb, int ldq, int tpos0, const float* __restrict__ rope, const float* __restrict__ qgain, ...
;     ...
; #pragma unroll
;     for (int ax = 0; ax < 2; ++ax) { const int pos = ax ? (t & 63) : (t >> 6);
; #pragma unroll
;       for (int q = 0; q < 2; ++q) { const int dl = 4 * ax + q, dh = dl + 2, p0 = q * 16 + 8 * hi;
;         const float* cp_ = rope + pos * 32 + p0; const float* gl = qgain + dl * 16 + 8 * hi; const float* gh = qgain + dh * 16 + 8 * hi;
;         float cs[8], sn[8], lo[8], hv[8];
; #pragma unroll
;         for (int i = 0; i < 8; ++i) { cs[i] = cp_[i]; sn[i] = cp_[4096 + i];
;           lo[i] = bf2f((unsigned)(unsigned short)qr[dl][i]) * rinv * gl[i]; hv[i] = bf2f((unsigned)(unsigned short)qr[dh][i]) * rinv * gh[i]; }
;         u32x4 wl, wh;
; #pragma unroll
;         for (int i = 0; i < 4; ++i) { const float l0 = lo[2 * i] * cs[2 * i] - hv[2 * i] * sn[2 * i], l1 = lo[2 * i + 1] * cs[2 * i + 1] - hv[2 * i + 1] * sn[2 * i + 1];
;           const float h0 = hv[2 * i] * cs[2 * i] + lo[2 * i] * sn[2 * i], h1 = hv[2 * i + 1] * cs[2 * i + 1] + lo[2 * i + 1] * sn[2 * i + 1];
;           wl[i] = pk2(l0, l1); wh[i] = pk2(h0, h1); }
;         qr[dl] = *reinterpret_cast<bf16x8*>(&wl); qr[dh] = *reinterpret_cast<bf16x8*>(&wh); } } }
	v_mov_b32_e32 v29, v20
	v_pk_mul_f32 v[28:29], v[28:29], v[76:77]
	s_nop 0
	v_sub_f32_e32 v19, v28, v29
	v_mov_b32_e32 v28, v3
	v_mov_b32_e32 v29, v21
	v_pk_mul_f32 v[28:29], v[28:29], v[78:79]
	s_nop 0
	v_sub_f32_e32 v31, v28, v29
	v_mov_b32_e32 v29, v2
	v_mov_b32_e32 v2, v21
	v_mov_b32_e32 v28, v20
	v_pk_mul_f32 v[2:3], v[2:3], v[78:79]
	v_pk_mul_f32 v[28:29], v[28:29], v[76:77]
	v_add_f32_e32 v2, v2, v3
	v_add_f32_e32 v20, v28, v29
	v_cvt_pk_bf16_f32 v116, v20, v2
	v_mov_b32_e32 v2, v4
	v_mov_b32_e32 v3, v22
	v_pk_mul_f32 v[2:3], v[2:3], v[44:45]
	v_cvt_pk_bf16_f32 v120, v19, v31
	s_nop 0
	v_sub_f32_e32 v19, v2, v3
	v_mov_b32_e32 v2, v5
	v_mov_b32_e32 v3, v23
	v_pk_mul_f32 v[2:3], v[2:3], v[80:81]
	s_nop 0
	v_sub_f32_e32 v20, v2, v3
	v_mov_b32_e32 v2, v22
	v_mov_b32_e32 v3, v4
	v_pk_mul_f32 v[2:3], v[2:3], v[44:45]
	v_mov_b32_e32 v4, v23
	v_add_f32_e32 v21, v2, v3
	v_pk_mul_f32 v[2:3], v[4:5], v[80:81]
	v_cvt_pk_bf16_f32 v121, v19, v20
	s_waitcnt vmcnt(6)
	v_mov_b32_e32 v4, v14
	v_add_f32_e32 v2, v2, v3
	v_cvt_pk_bf16_f32 v117, v21, v2
	s_waitcnt vmcnt(4)
	v_mov_b32_e32 v5, v60
	v_mov_b32_e32 v60, v15
	v_pk_mul_f32 v[14:15], v[18:19], v[48:49] op_sel_hi:[0,1]
	v_mov_b32_e32 v20, v16
	v_mov_b32_e32 v21, v62
	v_pk_mul_f32 v[14:15], v[14:15], v[20:21]
	v_pk_mul_f32 v[20:21], v[18:19], v[46:47] op_sel_hi:[0,1]
	v_mov_b32_e32 v62, v17
	v_pk_mul_f32 v[16:17], v[20:21], v[62:63]
	v_pk_mul_f32 v[20:21], v[18:19], v[42:43] op_sel_hi:[0,1]
	v_mov_b32_e32 v22, v6
	v_mov_b32_e32 v23, v24
	v_pk_mul_f32 v[2:3], v[18:19], v[52:53] op_sel_hi:[0,1]
	v_pk_mul_f32 v[20:21], v[20:21], v[22:23]
	v_pk_mul_f32 v[22:23], v[18:19], v[40:41] op_sel_hi:[0,1]
	v_mov_b32_e32 v24, v7
	v_pk_mul_f32 v[2:3], v[2:3], v[4:5]
	v_pk_mul_f32 v[4:5], v[18:19], v[50:51] op_sel_hi:[0,1]
	v_pk_mul_f32 v[6:7], v[22:23], v[24:25]
	v_pk_mul_f32 v[22:23], v[18:19], v[38:39] op_sel_hi:[0,1]
	v_mov_b32_e32 v25, v26
	v_pk_mul_f32 v[18:19], v[18:19], v[36:37] op_sel_hi:[0,1]
	v_mov_b32_e32 v26, v9
	v_mov_b32_e32 v24, v8
	v_pk_mul_f32 v[8:9], v[18:19], v[26:27]
	s_waitcnt vmcnt(1)
	v_mov_b32_e32 v18, v68
	v_mov_b32_e32 v19, v10
	v_pk_mul_f32 v[18:19], v[18:19], v[2:3]
	v_pk_mul_f32 v[4:5], v[4:5], v[60:61]
	v_pk_mul_f32 v[22:23], v[22:23], v[24:25]
	v_sub_f32_e32 v24, v18, v19
	v_mov_b32_e32 v18, v69
	v_mov_b32_e32 v19, v11
	v_pk_mul_f32 v[18:19], v[18:19], v[4:5]
	s_nop 0
	v_sub_f32_e32 v25, v18, v19
	v_mov_b32_e32 v18, v10
	v_mov_b32_e32 v19, v68
	v_pk_mul_f32 v[2:3], v[18:19], v[2:3]
	v_mov_b32_e32 v68, v11
	v_add_f32_e32 v10, v2, v3
	v_pk_mul_f32 v[2:3], v[68:69], v[4:5]
	v_cvt_pk_bf16_f32 v126, v24, v25
	s_nop 0
	v_add_f32_e32 v2, v2, v3
	v_cvt_pk_bf16_f32 v122, v10, v2
	v_mov_b32_e32 v2, v70
	v_mov_b32_e32 v3, v12
	v_pk_mul_f32 v[2:3], v[2:3], v[14:15]
	s_nop 0
	v_sub_f32_e32 v4, v2, v3
	v_mov_b32_e32 v2, v71
	v_mov_b32_e32 v3, v13
	v_pk_mul_f32 v[2:3], v[2:3], v[16:17]
	s_nop 0
	v_sub_f32_e32 v5, v2, v3
	v_mov_b32_e32 v2, v12
	v_mov_b32_e32 v3, v70
	v_pk_mul_f32 v[2:3], v[2:3], v[14:15]
	v_mov_b32_e32 v70, v13
	v_add_f32_e32 v10, v2, v3
	v_pk_mul_f32 v[2:3], v[70:71], v[16:17]
	v_cvt_pk_bf16_f32 v127, v4, v5
	s_nop 0
	v_add_f32_e32 v2, v2, v3
	v_cvt_pk_bf16_f32 v123, v10, v2
	v_mov_b32_e32 v2, v64
	s_waitcnt vmcnt(0)
	v_mov_b32_e32 v3, v54
	v_pk_mul_f32 v[2:3], v[2:3], v[20:21]
	s_nop 0
	v_sub_f32_e32 v4, v2, v3
	v_mov_b32_e32 v2, v65
	v_mov_b32_e32 v3, v55
	v_pk_mul_f32 v[2:3], v[2:3], v[6:7]
	s_nop 0
	v_sub_f32_e32 v5, v2, v3
	v_mov_b32_e32 v2, v54
	v_mov_b32_e32 v3, v64
	v_pk_mul_f32 v[2:3], v[2:3], v[20:21]
	v_mov_b32_e32 v64, v55
	v_add_f32_e32 v10, v2, v3
	v_pk_mul_f32 v[2:3], v[64:65], v[6:7]
	v_cvt_pk_bf16_f32 v128, v4, v5
	s_nop 0
	v_add_f32_e32 v2, v2, v3
	v_cvt_pk_bf16_f32 v124, v10, v2
	v_mov_b32_e32 v2, v66
	v_mov_b32_e32 v3, v56
	v_pk_mul_f32 v[2:3], v[2:3], v[22:23]
	s_nop 0
	v_sub_f32_e32 v4, v2, v3
	v_mov_b32_e32 v2, v67
	v_mov_b32_e32 v3, v57
	v_pk_mul_f32 v[2:3], v[2:3], v[8:9]
	s_nop 0
	v_sub_f32_e32 v5, v2, v3
	v_mov_b32_e32 v2, v56
	v_mov_b32_e32 v3, v66
	v_pk_mul_f32 v[2:3], v[2:3], v[22:23]
	v_mov_b32_e32 v66, v57
	v_add_f32_e32 v6, v2, v3
	v_pk_mul_f32 v[2:3], v[66:67], v[8:9]
	v_cvt_pk_bf16_f32 v129, v4, v5
	s_nop 0
	v_add_f32_e32 v2, v2, v3
	v_cvt_pk_bf16_f32 v125, v6, v2

; __device__ __forceinline__ int otid() { int t = threadIdx.x; asm volatile("" : "+v"(t)); return t; }
; __device__ __forceinline__ unsigned xb_add(unsigned* p, unsigned v) { return __hip_atomic_fetch_add(p, v, __ATOMIC_RELAXED, __HIP_MEMORY_SCOPE_AGENT); }
; __device__ __forceinline__ int v_rd_base(int lane) { return ((lane & 3) << 3) | (((lane >> 2) & 3) << 6) | (((lane >> 4) & 1) << 5) | (((lane >> 5) & 1) << 8); }
; #define ATT_WAIT_BAR() asm volatile("s_waitcnt vmcnt(0) lgkmcnt(0)\n\ts_barrier" ::: "memory")
; __device__ __forceinline__ void attn_dma_body(const bf16_t* __restrict__ Qb, int ldq, int tpos0, const float* __restrict__ rope, const float* __restrict__ qgain, ...
;     ...
;   ATT_WAIT_BAR();
;   if (2 < NT) ATT_DMA(2, 2);
;   const int vb0 = (int)(uintptr_t)lds + 16384 + v_rd_base(lane);
;   f32x16 pA0, pA1, pB0, pB1; float mnA, mnB, alA, alB; bf16x8 pa0, pa1, pa2, pa3;
;   qkt(pA0, pA1, (const bf16_t*)lds, qr, r32, hi); partialSM(pA0, pA1, m_reg, mnA, alA);
; __global__ void __launch_bounds__(512, 2) mk_fwd(Params p_unused) {
;     ...
;             if (otid() == 0) { asm volatile("s_waitcnt vmcnt(0)" ::: "memory");
;                 (void)xb_add(WSP(unsigned, WS_CTL) + CW_DONE + 32 * (isl ? (b * 32 + rbk) : (64 + b)), 1u); }
.Lf16_noprio:
	s_waitcnt vmcnt(0) lgkmcnt(0)
	s_barrier
	s_cmp_lg_u32 s101, 0
	s_cbranch_scc0 .Ldc_skip
	s_mov_b32 s101, 0
	s_cmp_lg_u32 s42, 0
	s_cbranch_scc1 .Ldc_skip
	v_mov_b32_e32 v251, 1
	s_mov_b64 exec, 1
	global_atomic_add v163, v251, s[98:99]
	s_mov_b64 exec, -1
.Ldc_skip:
	s_add_u32 s2, s38, 0x8000
	s_addc_u32 s3, s39, 0
	s_add_u32 s4, s40, 0x8000
	s_addc_u32 s5, s41, 0
	s_add_i32 s6, s96, 0x10000
	s_add_i32 m0, s96, 0x10000
	s_nop 0
	global_load_lds_dwordx4 v170, s[2:3]
	s_add_i32 m0, s96, 0x12000
	s_nop 0
	global_load_lds_dwordx4 v172, s[2:3]
	s_add_i32 m0, s96, 0x14000
	s_nop 0
	global_load_lds_dwordx4 v171, s[2:3]
	s_add_i32 m0, s96, 0x16000
	s_nop 0
	global_load_lds_dwordx4 v173, s[2:3]
	s_add_u32 s2, s2, 0x4000
	s_addc_u32 s3, s3, 0
	v_add_u32_e32 v187, 0x10000, v183
	v_add_u32_e32 v188, 0x10000, v184
	v_add_u32_e32 v189, 0x10000, v185
	v_add_u32_e32 v190, 0x10000, v186
	v_add_u32_e32 v180, 0x10000, v191
	v_add_u32_e32 v181, 0x10000, v192
	s_mov_b32 s36, 0
	ds_read_b128 v[146:149], v183 offset:0
	ds_read_b128 v[150:153], v183 offset:4096
	ds_read_b128 v[154:157], v183 offset:8192
	ds_read_b128 v[158:161], v183 offset:12288
	ds_read_b128 v[198:201], v184 offset:0
	ds_read_b128 v[202:205], v184 offset:4096
	ds_read_b128 v[206:209], v184 offset:8192
	ds_read_b128 v[210:213], v184 offset:12288
	s_waitcnt lgkmcnt(6)
	v_mfma_f32_16x16x32_bf16 v[66:69], v[146:149], v[98:101], 0
	v_mfma_f32_16x16x32_bf16 v[70:73], v[146:149], v[114:117], 0
	v_mfma_f32_16x16x32_bf16 v[74:77], v[150:153], v[98:101], 0
	v_mfma_f32_16x16x32_bf16 v[78:81], v[150:153], v[114:117], 0
	ds_read_b128 v[146:149], v185 offset:0
	ds_read_b128 v[150:153], v185 offset:4096
	s_waitcnt lgkmcnt(6)
	v_mfma_f32_16x16x32_bf16 v[82:85], v[154:157], v[98:101], 0
	v_mfma_f32_16x16x32_bf16 v[86:89], v[154:157], v[114:117], 0
	v_mfma_f32_16x16x32_bf16 v[90:93], v[158:161], v[98:101], 0
	v_mfma_f32_16x16x32_bf16 v[94:97], v[158:161], v[114:117], 0
	ds_read_b128 v[154:157], v185 offset:8192
	ds_read_b128 v[158:161], v185 offset:12288
	s_waitcnt lgkmcnt(6)
	v_mfma_f32_16x16x32_bf16 v[66:69], v[198:201], v[102:105], v[66:69]
	v_mfma_f32_16x16x32_bf16 v[70:73], v[198:201], v[118:121], v[70:73]
	v_mfma_f32_16x16x32_bf16 v[74:77], v[202:205], v[102:105], v[74:77]
	v_mfma_f32_16x16x32_bf16 v[78:81], v[202:205], v[118:121], v[78:81]
	ds_read_b128 v[198:201], v186 offset:0
	ds_read_b128 v[202:205], v186 offset:4096
	s_waitcnt lgkmcnt(6)
	v_mfma_f32_16x16x32_bf16 v[82:85], v[206:209], v[102:105], v[82:85]
	v_mfma_f32_16x16x32_bf16 v[86:89], v[206:209], v[118:121], v[86:89]
	v_mfma_f32_16x16x32_bf16 v[90:93], v[210:213], v[102:105], v[90:93]
	v_mfma_f32_16x16x32_bf16 v[94:97], v[210:213], v[118:121], v[94:97]
	ds_read_b128 v[206:209], v186 offset:8192
	ds_read_b128 v[210:213], v186 offset:12288
	s_waitcnt lgkmcnt(6)
	v_mfma_f32_16x16x32_bf16 v[66:69], v[146:149], v[106:109], v[66:69]
	v_mfma_f32_16x16x32_bf16 v[70:73], v[146:149], v[122:125], v[70:73]
	v_mfma_f32_16x16x32_bf16 v[74:77], v[150:153], v[106:109], v[74:77]
	v_mfma_f32_16x16x32_bf16 v[78:81], v[150:153], v[122:125], v[78:81]
	s_waitcnt lgkmcnt(4)
	v_mfma_f32_16x16x32_bf16 v[82:85], v[154:157], v[106:109], v[82:85]
	v_mfma_f32_16x16x32_bf16 v[86:89], v[154:157], v[122:125], v[86:89]
	v_mfma_f32_16x16x32_bf16 v[90:93], v[158:161], v[106:109], v[90:93]
	v_mfma_f32_16x16x32_bf16 v[94:97], v[158:161], v[122:125], v[94:97]
	s_waitcnt lgkmcnt(2)
	v_mfma_f32_16x16x32_bf16 v[66:69], v[198:201], v[110:113], v[66:69]
	v_mfma_f32_16x16x32_bf16 v[70:73], v[198:201], v[126:129], v[70:73]
	v_mfma_f32_16x16x32_bf16 v[74:77], v[202:205], v[110:113], v[74:77]
	v_mfma_f32_16x16x32_bf16 v[78:81], v[202:205], v[126:129], v[78:81]
	s_waitcnt lgkmcnt(0)
	v_mfma_f32_16x16x32_bf16 v[82:85], v[206:209], v[110:113], v[82:85]
	v_mfma_f32_16x16x32_bf16 v[86:89], v[206:209], v[126:129], v[86:89]
	v_mfma_f32_16x16x32_bf16 v[90:93], v[210:213], v[110:113], v[90:93]
	v_mfma_f32_16x16x32_bf16 v[94:97], v[210:213], v[126:129], v[94:97]
	s_nop 7
	v_exp_f32_e32 v66, v66
	v_exp_f32_e32 v67, v67
	v_exp_f32_e32 v68, v68
	v_exp_f32_e32 v69, v69
	v_exp_f32_e32 v70, v70
	v_exp_f32_e32 v71, v71
	v_exp_f32_e32 v72, v72
	v_exp_f32_e32 v73, v73
	v_exp_f32_e32 v74, v74
	v_exp_f32_e32 v75, v75
	v_exp_f32_e32 v76, v76
	v_exp_f32_e32 v77, v77
	v_exp_f32_e32 v78, v78
	v_exp_f32_e32 v79, v79
	v_exp_f32_e32 v80, v80
	v_exp_f32_e32 v81, v81
	v_exp_f32_e32 v82, v82
	v_exp_f32_e32 v83, v83
	v_exp_f32_e32 v84, v84
	v_exp_f32_e32 v85, v85
	v_exp_f32_e32 v86, v86
	v_exp_f32_e32 v87, v87
	v_exp_f32_e32 v88, v88
	v_exp_f32_e32 v89, v89
	v_exp_f32_e32 v90, v90
	v_exp_f32_e32 v91, v91
	v_exp_f32_e32 v92, v92
	v_exp_f32_e32 v93, v93
	v_exp_f32_e32 v94, v94
	v_exp_f32_e32 v95, v95
	v_exp_f32_e32 v96, v96
	v_exp_f32_e32 v97, v97
	v_cvt_pk_bf16_f32 v130, v66, v67
	v_cvt_pk_bf16_f32 v131, v68, v69
	v_cvt_pk_bf16_f32 v132, v74, v75
	v_cvt_pk_bf16_f32 v133, v76, v77
	v_cvt_pk_bf16_f32 v134, v82, v83
	v_cvt_pk_bf16_f32 v135, v84, v85
	v_cvt_pk_bf16_f32 v136, v90, v91
	v_cvt_pk_bf16_f32 v137, v92, v93
	v_cvt_pk_bf16_f32 v138, v70, v71
	v_cvt_pk_bf16_f32 v139, v72, v73
	v_cvt_pk_bf16_f32 v140, v78, v79
	v_cvt_pk_bf16_f32 v141, v80, v81
	v_cvt_pk_bf16_f32 v142, v86, v87
	v_cvt_pk_bf16_f32 v143, v88, v89
	v_cvt_pk_bf16_f32 v144, v94, v95
	v_cvt_pk_bf16_f32 v145, v96, v97
	s_mov_b32 s97, 1
	s_cmp_lt_u32 s42, 4
	s_cbranch_scc1 .Lf16_L_loop
	.p2align 6

; #define SBAR() __builtin_amdgcn_sched_barrier(0)
; __device__ __forceinline__ int crow(int r, int hi) { return (r & 3) + 8 * (r >> 2) + 4 * hi; }
; #define RESC(a) do { if (__any((a) < 1.f)) { if (hi == 0) al_l[r32] = (a); asm volatile("s_waitcnt lgkmcnt(0)" ::: "memory"); \
;     for (int d = 0; d < 4; ++d) for (int r = 0; r < 16; ++r) o[d][r] *= al_l[crow(r, hi)]; } } while (0)
; #define RESC(a) do { if (__any((a) < 1.f)) { if (hi == 0) al_l[r32] = (a); asm volatile("s_waitcnt lgkmcnt(0)" ::: "memory"); \
;     for (int d = 0; d < 4; ++d) for (int r = 0; r < 16; ++r) o[d][r] *= al_l[crow(r, hi)]; } } while (0)
; __device__ __forceinline__ void attn_dma_body(const bf16_t* __restrict__ Qb, int ldq, int tpos0, const float* __restrict__ rope, const float* __restrict__ qgain, ...
;     ...
;   { SBAR(); qkt(pB0, pB1, (const bf16_t*)(lds + ((NT - 1) & 3) * SHM_SLOT), qr, r32, hi);
;     finishSM(pA0, pA1, alA, l_reg, pa0, pa1, pa2, pa3); SBAR();
;     pv_d0(o, vb0 + ((NT - 2) & 3) * (int)SHM_SLOT, pa0, pa1, pa2, pa3); partialSM(pB0, pB1, m_reg, mnB, alB);
;     RESC(alB);
;     finishSM(pB0, pB1, alB, l_reg, pa0, pa1, pa2, pa3); SBAR();
;     pv_d0(o, vb0 + ((NT - 1) & 3) * (int)SHM_SLOT, pa0, pa1, pa2, pa3); }
;   if (hi == 0) li_l[r32] = l_reg; asm volatile("s_waitcnt lgkmcnt(0)" ::: "memory");
;   float rli[16];
; #pragma unroll
;   for (int r = 0; r < 16; ++r) rli[r] = __builtin_amdgcn_rcpf(li_l[crow(r, hi)]);
;   bf16_t* Ow = Ob + (long)(wid * QBLK) * LDO;
;   asm volatile("s_waitcnt lgkmcnt(0)\n\ts_barrier" ::: "memory");
.Lf16_done:
	s_mov_b32 s37, 0x18000
	ds_read_b64_tr_b16 v[214:215], v180 offset:32768
	ds_read_b64_tr_b16 v[216:217], v180 offset:36864
	ds_read_b64_tr_b16 v[218:219], v181 offset:32768
	ds_read_b64_tr_b16 v[220:221], v181 offset:36864
	ds_read_b64_tr_b16 v[222:223], v180 offset:33280
	ds_read_b64_tr_b16 v[224:225], v180 offset:37376
	ds_read_b64_tr_b16 v[226:227], v181 offset:33280
	ds_read_b64_tr_b16 v[228:229], v181 offset:37376
	ds_read_b64_tr_b16 v[230:231], v180 offset:33792
	ds_read_b64_tr_b16 v[232:233], v180 offset:37888
	ds_read_b64_tr_b16 v[234:235], v181 offset:33792
	ds_read_b64_tr_b16 v[236:237], v181 offset:37888
	s_waitcnt lgkmcnt(8)
	v_mfma_f32_16x16x32_bf16 v[2:5], v[214:217], v[130:133], v[2:5]
	v_mfma_f32_16x16x32_bf16 v[6:9], v[214:217], v[138:141], v[6:9]
	v_mfma_f32_16x16x32_bf16 v[10:13], v[218:221], v[130:133], v[10:13]
	v_mfma_f32_16x16x32_bf16 v[14:17], v[218:221], v[138:141], v[14:17]
	ds_read_b64_tr_b16 v[238:239], v180 offset:34304
	ds_read_b64_tr_b16 v[240:241], v180 offset:38400
	ds_read_b64_tr_b16 v[242:243], v181 offset:34304
	ds_read_b64_tr_b16 v[244:245], v181 offset:38400
	s_waitcnt lgkmcnt(8)
	v_mfma_f32_16x16x32_bf16 v[18:21], v[222:225], v[130:133], v[18:21]
	v_mfma_f32_16x16x32_bf16 v[22:25], v[222:225], v[138:141], v[22:25]
	v_mfma_f32_16x16x32_bf16 v[26:29], v[226:229], v[130:133], v[26:29]
	v_mfma_f32_16x16x32_bf16 v[30:33], v[226:229], v[138:141], v[30:33]
	v_mfma_f32_16x16x32_bf16 v[246:249], v[194:197], v[130:133], v[246:249]
	ds_read_b64_tr_b16 v[214:215], v180 offset:40960
	ds_read_b64_tr_b16 v[216:217], v180 offset:45056
	ds_read_b64_tr_b16 v[218:219], v181 offset:40960
	ds_read_b64_tr_b16 v[220:221], v181 offset:45056
	s_waitcnt lgkmcnt(8)
	v_mfma_f32_16x16x32_bf16 v[34:37], v[230:233], v[130:133], v[34:37]
	v_mfma_f32_16x16x32_bf16 v[38:41], v[230:233], v[138:141], v[38:41]
	v_mfma_f32_16x16x32_bf16 v[42:45], v[234:237], v[130:133], v[42:45]
	v_mfma_f32_16x16x32_bf16 v[46:49], v[234:237], v[138:141], v[46:49]
	ds_read_b64_tr_b16 v[222:223], v180 offset:41472
	ds_read_b64_tr_b16 v[224:225], v180 offset:45568
	ds_read_b64_tr_b16 v[226:227], v181 offset:41472
	ds_read_b64_tr_b16 v[228:229], v181 offset:45568
	s_waitcnt lgkmcnt(8)
	v_mfma_f32_16x16x32_bf16 v[50:53], v[238:241], v[130:133], v[50:53]
	v_mfma_f32_16x16x32_bf16 v[54:57], v[238:241], v[138:141], v[54:57]
	v_mfma_f32_16x16x32_bf16 v[58:61], v[242:245], v[130:133], v[58:61]
	v_mfma_f32_16x16x32_bf16 v[62:65], v[242:245], v[138:141], v[62:65]
	v_mfma_f32_16x16x32_bf16 v[252:255], v[194:197], v[138:141], v[252:255]
	ds_read_b64_tr_b16 v[230:231], v180 offset:41984
	ds_read_b64_tr_b16 v[232:233], v180 offset:46080
	ds_read_b64_tr_b16 v[234:235], v181 offset:41984
	ds_read_b64_tr_b16 v[236:237], v181 offset:46080
	s_waitcnt lgkmcnt(8)
	v_mfma_f32_16x16x32_bf16 v[2:5], v[214:217], v[134:137], v[2:5]
	v_mfma_f32_16x16x32_bf16 v[6:9], v[214:217], v[142:145], v[6:9]
	v_mfma_f32_16x16x32_bf16 v[10:13], v[218:221], v[134:137], v[10:13]
	v_mfma_f32_16x16x32_bf16 v[14:17], v[218:221], v[142:145], v[14:17]
	ds_read_b64_tr_b16 v[238:239], v180 offset:42496
	ds_read_b64_tr_b16 v[240:241], v180 offset:46592
	ds_read_b64_tr_b16 v[242:243], v181 offset:42496
	ds_read_b64_tr_b16 v[244:245], v181 offset:46592
	s_waitcnt lgkmcnt(8)
	v_mfma_f32_16x16x32_bf16 v[18:21], v[222:225], v[134:137], v[18:21]
	v_mfma_f32_16x16x32_bf16 v[22:25], v[222:225], v[142:145], v[22:25]
	v_mfma_f32_16x16x32_bf16 v[26:29], v[226:229], v[134:137], v[26:29]
	v_mfma_f32_16x16x32_bf16 v[30:33], v[226:229], v[142:145], v[30:33]
	v_mfma_f32_16x16x32_bf16 v[246:249], v[194:197], v[134:137], v[246:249]
	s_waitcnt lgkmcnt(4)
	v_mfma_f32_16x16x32_bf16 v[34:37], v[230:233], v[134:137], v[34:37]
	v_mfma_f32_16x16x32_bf16 v[38:41], v[230:233], v[142:145], v[38:41]
	v_mfma_f32_16x16x32_bf16 v[42:45], v[234:237], v[134:137], v[42:45]
	v_mfma_f32_16x16x32_bf16 v[46:49], v[234:237], v[142:145], v[46:49]
	s_waitcnt lgkmcnt(0)
	v_mfma_f32_16x16x32_bf16 v[50:53], v[238:241], v[134:137], v[50:53]
	v_mfma_f32_16x16x32_bf16 v[54:57], v[238:241], v[142:145], v[54:57]
	v_mfma_f32_16x16x32_bf16 v[58:61], v[242:245], v[134:137], v[58:61]
	v_mfma_f32_16x16x32_bf16 v[62:65], v[242:245], v[142:145], v[62:65]
	v_mfma_f32_16x16x32_bf16 v[252:255], v[194:197], v[142:145], v[252:255]
	s_nop 7
	s_nop 7
	v_mov_b32_e32 v182, v246
	v_mov_b32_e32 v195, v252
	v_rcp_f32_e32 v182, v182
	v_rcp_f32_e32 v195, v195
	s_waitcnt lgkmcnt(0)
	s_barrier
; __device__ __forceinline__ unsigned f2bf(float f) { unsigned u = __builtin_bit_cast(unsigned, f); return (u + 0x7fffu + ((u >> 16) & 1u)) >> 16; }
; __device__ __forceinline__ int otid() { int t = threadIdx.x; asm volatile("" : "+v"(t)); return t; }
; __device__ __forceinline__ unsigned xb_add(unsigned* p, unsigned v) { return __hip_atomic_fetch_add(p, v, __ATOMIC_RELAXED, __HIP_MEMORY_SCOPE_AGENT); }
; __device__ __forceinline__ int crow(int r, int hi) { return (r & 3) + 8 * (r >> 2) + 4 * hi; }
; #define ATT_WAIT_BAR() asm volatile("s_waitcnt vmcnt(0) lgkmcnt(0)\n\ts_barrier" ::: "memory")
; __device__ __forceinline__ void attn_dma_body(const bf16_t* __restrict__ Qb, int ldq, int tpos0, const float* __restrict__ rope, const float* __restrict__ qgain, ...
;     ...
;   { char* st = lds + wid * 8704;
; #pragma unroll
;     for (int r = 0; r < 16; ++r) { const int orow = crow(r, hi);
; #pragma unroll
;       for (int d0 = 0; d0 < 4; ++d0) *(bf16_t*)(st + orow * 272 + (d0 * 32 + r32) * 2) = (bf16_t)f2bf(o[d0][r] * rli[r]); }
;     asm volatile("s_waitcnt lgkmcnt(0)" ::: "memory");
; #pragma unroll
;     for (int i = 0; i < 8; ++i) { const int c = i * 64 + lane, row = c >> 4, cc = c & 15; const u32x4 v = *(const u32x4*)(st + row * 272 + cc * 16);
;       const bf16_t* gp = Ow + (long)row * LDO + cc * 8;
;       asm volatile("global_store_dwordx4 %0, %1, off sc1\n\ts_nop 1" :: "v"(gp), "v"(v) : "memory"); } }
;   ATT_WAIT_BAR();
; __global__ void __launch_bounds__(512, 2) mk_fwd(Params p_unused) {
;     ...
;             if (otid() == 0) { asm volatile("s_waitcnt vmcnt(0)" ::: "memory");
;                 (void)xb_add(WSP(unsigned, WS_CTL) + CW_DONE + 32 * (isl ? (b * 32 + rbk) : (64 + b)), 1u); }
	v_mul_u32_u24_e32 v84, 0x2200, v179
	v_and_b32_e32 v246, 15, v167
	v_lshrrev_b32_e32 v247, 4, v167
	v_mul_u32_u24_e32 v248, 0x110, v246
	v_add_u32_e32 v248, v248, v84
	v_lshl_add_u32 v248, v247, 3, v248
	v_mul_f32_e32 v2, v2, v182
	v_mul_f32_e32 v3, v3, v182
	v_mul_f32_e32 v4, v4, v182
	v_mul_f32_e32 v5, v5, v182
	v_cvt_pk_bf16_f32 v252, v2, v3
	v_cvt_pk_bf16_f32 v253, v4, v5
	ds_write_b64 v248, v[252:253] offset:0
	v_mul_f32_e32 v6, v6, v195
	v_mul_f32_e32 v7, v7, v195
	v_mul_f32_e32 v8, v8, v195
	v_mul_f32_e32 v9, v9, v195
	v_cvt_pk_bf16_f32 v254, v6, v7
	v_cvt_pk_bf16_f32 v255, v8, v9
	ds_write_b64 v248, v[254:255] offset:4352
	v_mul_f32_e32 v10, v10, v182
	v_mul_f32_e32 v11, v11, v182
	v_mul_f32_e32 v12, v12, v182
	v_mul_f32_e32 v13, v13, v182
	v_cvt_pk_bf16_f32 v252, v10, v11
	v_cvt_pk_bf16_f32 v253, v12, v13
	ds_write_b64 v248, v[252:253] offset:32
	v_mul_f32_e32 v14, v14, v195
	v_mul_f32_e32 v15, v15, v195
	v_mul_f32_e32 v16, v16, v195
	v_mul_f32_e32 v17, v17, v195
	v_cvt_pk_bf16_f32 v254, v14, v15
	v_cvt_pk_bf16_f32 v255, v16, v17
	ds_write_b64 v248, v[254:255] offset:4384
	v_mul_f32_e32 v18, v18, v182
	v_mul_f32_e32 v19, v19, v182
	v_mul_f32_e32 v20, v20, v182
	v_mul_f32_e32 v21, v21, v182
	v_cvt_pk_bf16_f32 v252, v18, v19
	v_cvt_pk_bf16_f32 v253, v20, v21
	ds_write_b64 v248, v[252:253] offset:64
	v_mul_f32_e32 v22, v22, v195
	v_mul_f32_e32 v23, v23, v195
	v_mul_f32_e32 v24, v24, v195
	v_mul_f32_e32 v25, v25, v195
	v_cvt_pk_bf16_f32 v254, v22, v23
	v_cvt_pk_bf16_f32 v255, v24, v25
	ds_write_b64 v248, v[254:255] offset:4416
	v_mul_f32_e32 v26, v26, v182
	v_mul_f32_e32 v27, v27, v182
	v_mul_f32_e32 v28, v28, v182
	v_mul_f32_e32 v29, v29, v182
	v_cvt_pk_bf16_f32 v252, v26, v27
	v_cvt_pk_bf16_f32 v253, v28, v29
	ds_write_b64 v248, v[252:253] offset:96
	v_mul_f32_e32 v30, v30, v195
	v_mul_f32_e32 v31, v31, v195
	v_mul_f32_e32 v32, v32, v195
	v_mul_f32_e32 v33, v33, v195
	v_cvt_pk_bf16_f32 v254, v30, v31
	v_cvt_pk_bf16_f32 v255, v32, v33
	ds_write_b64 v248, v[254:255] offset:4448
	v_mul_f32_e32 v34, v34, v182
	v_mul_f32_e32 v35, v35, v182
	v_mul_f32_e32 v36, v36, v182
	v_mul_f32_e32 v37, v37, v182
	v_cvt_pk_bf16_f32 v252, v34, v35
	v_cvt_pk_bf16_f32 v253, v36, v37
	ds_write_b64 v248, v[252:253] offset:128
	v_mul_f32_e32 v38, v38, v195
	v_mul_f32_e32 v39, v39, v195
	v_mul_f32_e32 v40, v40, v195
	v_mul_f32_e32 v41, v41, v195
	v_cvt_pk_bf16_f32 v254, v38, v39
	v_cvt_pk_bf16_f32 v255, v40, v41
	ds_write_b64 v248, v[254:255] offset:4480
	v_mul_f32_e32 v42, v42, v182
	v_mul_f32_e32 v43, v43, v182
	v_mul_f32_e32 v44, v44, v182
	v_mul_f32_e32 v45, v45, v182
	v_cvt_pk_bf16_f32 v252, v42, v43
	v_cvt_pk_bf16_f32 v253, v44, v45
	ds_write_b64 v248, v[252:253] offset:160
	v_mul_f32_e32 v46, v46, v195
	v_mul_f32_e32 v47, v47, v195
	v_mul_f32_e32 v48, v48, v195
	v_mul_f32_e32 v49, v49, v195
	v_cvt_pk_bf16_f32 v254, v46, v47
	v_cvt_pk_bf16_f32 v255, v48, v49
	ds_write_b64 v248, v[254:255] offset:4512
	v_mul_f32_e32 v50, v50, v182
	v_mul_f32_e32 v51, v51, v182
	v_mul_f32_e32 v52, v52, v182
	v_mul_f32_e32 v53, v53, v182
	v_cvt_pk_bf16_f32 v252, v50, v51
	v_cvt_pk_bf16_f32 v253, v52, v53
	ds_write_b64 v248, v[252:253] offset:192
	v_mul_f32_e32 v54, v54, v195
	v_mul_f32_e32 v55, v55, v195
	v_mul_f32_e32 v56, v56, v195
	v_mul_f32_e32 v57, v57, v195
	v_cvt_pk_bf16_f32 v254, v54, v55
	v_cvt_pk_bf16_f32 v255, v56, v57
	ds_write_b64 v248, v[254:255] offset:4544
	v_mul_f32_e32 v58, v58, v182
	v_mul_f32_e32 v59, v59, v182
	v_mul_f32_e32 v60, v60, v182
	v_mul_f32_e32 v61, v61, v182
	v_cvt_pk_bf16_f32 v252, v58, v59
	v_cvt_pk_bf16_f32 v253, v60, v61
	ds_write_b64 v248, v[252:253] offset:224
	v_mul_f32_e32 v62, v62, v195
	v_mul_f32_e32 v63, v63, v195
	v_mul_f32_e32 v64, v64, v195
	v_mul_f32_e32 v65, v65, v195
	v_cvt_pk_bf16_f32 v254, v62, v63
	v_cvt_pk_bf16_f32 v255, v64, v65
	ds_write_b64 v248, v[254:255] offset:4576
	s_waitcnt lgkmcnt(0)
	s_lshl_b64 s[6:7], s[70:71], 12
	s_add_u32 s6, s23, s6
	s_addc_u32 s7, s94, s7
	s_add_u32 s6, s6, s44
	s_addc_u32 s7, s7, s45
	v_ashrrev_i32_e32 v165, 31, v164
	v_lshlrev_b64 v[66:67], 12, v[164:165]
	v_lshl_add_u64 v[6:7], s[6:7], 0, v[66:67]
	v_lshlrev_b32_e32 v162, 4, v246
	v_lshl_add_u64 v[6:7], v[6:7], 0, v[162:163]
	v_lshlrev_b32_e32 v162, 12, v247
	v_lshl_add_u64 v[6:7], v[6:7], 0, v[162:163]
	v_mul_u32_u24_e32 v249, 0x110, v247
	v_add_u32_e32 v249, v249, v84
	v_lshl_add_u32 v249, v246, 4, v249
	ds_read_b128 v[66:69], v249 offset:0
	ds_read_b128 v[70:73], v249 offset:1088
	ds_read_b128 v[74:77], v249 offset:2176
	ds_read_b128 v[78:81], v249 offset:3264
	ds_read_b128 v[82:85], v249 offset:4352
	ds_read_b128 v[86:89], v249 offset:5440
	ds_read_b128 v[90:93], v249 offset:6528
	ds_read_b128 v[94:97], v249 offset:7616
	s_mov_b64 s[8:9], 0x0
	v_lshl_add_u64 v[8:9], v[6:7], 0, s[8:9]
	s_waitcnt lgkmcnt(7)
	global_store_dwordx4 v[8:9], v[66:69], off sc1
	s_mov_b64 s[8:9], 0x4000
	v_lshl_add_u64 v[98:99], v[6:7], 0, s[8:9]
	s_waitcnt lgkmcnt(6)
	global_store_dwordx4 v[98:99], v[70:73], off sc1
	s_mov_b64 s[8:9], 0x8000
	v_lshl_add_u64 v[8:9], v[6:7], 0, s[8:9]
	s_waitcnt lgkmcnt(5)
	global_store_dwordx4 v[8:9], v[74:77], off sc1
	s_mov_b64 s[8:9], 0xc000
	v_lshl_add_u64 v[98:99], v[6:7], 0, s[8:9]
	s_waitcnt lgkmcnt(4)
	global_store_dwordx4 v[98:99], v[78:81], off sc1
	s_mov_b64 s[8:9], 0x10000
	v_lshl_add_u64 v[8:9], v[6:7], 0, s[8:9]
	s_waitcnt lgkmcnt(3)
	global_store_dwordx4 v[8:9], v[82:85], off sc1
	s_mov_b64 s[8:9], 0x14000
	v_lshl_add_u64 v[98:99], v[6:7], 0, s[8:9]
	s_waitcnt lgkmcnt(2)
	global_store_dwordx4 v[98:99], v[86:89], off sc1
	s_mov_b64 s[8:9], 0x18000
	v_lshl_add_u64 v[8:9], v[6:7], 0, s[8:9]
	s_waitcnt lgkmcnt(1)
	global_store_dwordx4 v[8:9], v[90:93], off sc1
	s_mov_b64 s[8:9], 0x1c000
	v_lshl_add_u64 v[98:99], v[6:7], 0, s[8:9]
	s_waitcnt lgkmcnt(0)
	global_store_dwordx4 v[98:99], v[94:97], off sc1
	s_mov_b32 s101, 0
	s_and_b64 vcc, exec, s[12:13]
	s_cbranch_vccz .Ldc_no
	s_cmp_lt_i32 s21, 24
	s_cselect_b32 s6, 4, 3
	s_cmp_lt_u32 s95, s6
	s_cbranch_scc0 .Ldc_no
	s_mov_b32 s101, 1
	s_lshl_b32 s98, s64, 5
	s_add_i32 s98, s98, s68
	s_lshl_b32 s98, s98, 7
	s_add_u32 s98, s98, 0x8000
	s_add_u32 s98, s28, s98
	s_addc_u32 s99, s29, 0
	s_waitcnt lgkmcnt(0)
	s_barrier
	v_readlane_b32 s96, v250, 4
	v_readlane_b32 s97, v250, 5
	s_setprio 0
	s_mov_b64 s[2:3], 0
	s_branch .LBB0_376
.Ldc_no:
	s_waitcnt vmcnt(0) lgkmcnt(0)
	s_barrier
	v_readlane_b32 s96, v250, 4
	v_readlane_b32 s97, v250, 5
	s_setprio 0
	s_branch .LBB0_437
